# P6 batch builder: every token's 128 range-sorted entries cut into 16 full batches of 8 (no dummy rows), the 128 batches of a group ordered by the range of their first row so the sweep stays range-alig
# speedup vs baseline: 1.0084x; 1.0084x over previous
.LBB0_936:
	s_or_b64 exec, exec, s[0:1]
	v_cmp_lt_i32_e32 vcc, -1, v35
	s_movk_i32 s0, 0xff00
	v_lshl_add_u32 v25, v25, 2, s85
	v_cndmask_b32_e64 v44, v211, -1, vcc
	v_cmp_lt_i32_e32 vcc, -1, v34
	v_bitop3_b32 v35, v44, v35, s0 bitop3:0x78
	v_sub_f32_e32 v44, v35, v35
	v_cndmask_b32_e64 v88, v211, -1, vcc
	v_cmp_lt_i32_e32 vcc, -1, v33
	v_bitop3_b32 v34, v88, v34, s0 bitop3:0x78
	v_mul_f32_e32 v44, 0x3fb8aa3b, v44
	v_cndmask_b32_e64 v88, v211, -1, vcc
	v_cmp_lt_i32_e32 vcc, -1, v32
	v_sub_f32_e32 v34, v34, v35
	v_bitop3_b32 v33, v88, v33, s0 bitop3:0x78
	v_cndmask_b32_e64 v88, v211, -1, vcc
	v_cmp_lt_i32_e32 vcc, -1, v30
	v_exp_f32_e32 v44, v44
	v_mul_f32_e32 v34, 0x3fb8aa3b, v34
	v_sub_f32_e32 v33, v33, v35
	v_bitop3_b32 v32, v88, v32, s0 bitop3:0x78
	v_cndmask_b32_e64 v89, v211, -1, vcc
	v_cmp_lt_i32_e32 vcc, -1, v28
	v_exp_f32_e32 v34, v34
	v_mul_f32_e32 v33, 0x3fb8aa3b, v33
	v_sub_f32_e32 v32, v32, v35
	v_bitop3_b32 v30, v89, v30, s0 bitop3:0x78
	v_cndmask_b32_e64 v89, v211, -1, vcc
	v_cmp_lt_i32_e32 vcc, -1, v26
	v_exp_f32_e32 v33, v33
	v_mul_f32_e32 v32, 0x3fb8aa3b, v32
	v_sub_f32_e32 v30, v30, v35
	v_bitop3_b32 v28, v89, v28, s0 bitop3:0x78
	v_cndmask_b32_e64 v89, v211, -1, vcc
	v_cmp_lt_i32_e32 vcc, -1, v23
	v_exp_f32_e32 v32, v32
	v_mul_f32_e32 v30, 0x3fb8aa3b, v30
	v_sub_f32_e32 v28, v28, v35
	v_bitop3_b32 v26, v89, v26, s0 bitop3:0x78
	v_cndmask_b32_e64 v89, v211, -1, vcc
	v_cmp_lt_i32_e32 vcc, -1, v22
	v_add_f32_e32 v88, 0, v44
	v_exp_f32_e32 v30, v30
	v_mul_f32_e32 v28, 0x3fb8aa3b, v28
	v_sub_f32_e32 v26, v26, v35
	v_bitop3_b32 v23, v89, v23, s0 bitop3:0x78
	v_cndmask_b32_e64 v89, v211, -1, vcc
	v_cmp_lt_i32_e32 vcc, -1, v20
	v_add_f32_e32 v88, v88, v34
	v_exp_f32_e32 v28, v28
	v_mul_f32_e32 v26, 0x3fb8aa3b, v26
	v_sub_f32_e32 v23, v23, v35
	v_bitop3_b32 v22, v89, v22, s0 bitop3:0x78
	v_cndmask_b32_e64 v89, v211, -1, vcc
	v_cmp_lt_i32_e32 vcc, -1, v18
	v_add_f32_e32 v88, v88, v33
	v_exp_f32_e32 v26, v26
	v_mul_f32_e32 v23, 0x3fb8aa3b, v23
	v_sub_f32_e32 v22, v22, v35
	v_bitop3_b32 v20, v89, v20, s0 bitop3:0x78
	v_cndmask_b32_e64 v89, v211, -1, vcc
	v_cmp_lt_i32_e32 vcc, -1, v16
	v_add_f32_e32 v88, v88, v32
	v_exp_f32_e32 v23, v23
	v_mul_f32_e32 v22, 0x3fb8aa3b, v22
	v_sub_f32_e32 v20, v20, v35
	v_bitop3_b32 v18, v89, v18, s0 bitop3:0x78
	v_cndmask_b32_e64 v89, v211, -1, vcc
	v_cmp_lt_i32_e32 vcc, -1, v14
	v_add_f32_e32 v88, v88, v30
	v_exp_f32_e32 v22, v22
	v_mul_f32_e32 v20, 0x3fb8aa3b, v20
	v_sub_f32_e32 v18, v18, v35
	v_bitop3_b32 v16, v89, v16, s0 bitop3:0x78
	v_cndmask_b32_e64 v89, v211, -1, vcc
	v_cmp_lt_i32_e32 vcc, -1, v13
	v_add_f32_e32 v88, v88, v28
	v_exp_f32_e32 v20, v20
	v_mul_f32_e32 v18, 0x3fb8aa3b, v18
	v_sub_f32_e32 v16, v16, v35
	v_bitop3_b32 v14, v89, v14, s0 bitop3:0x78
	v_cndmask_b32_e64 v89, v211, -1, vcc
	v_cmp_lt_i32_e32 vcc, -1, v11
	v_add_f32_e32 v88, v88, v26
	v_exp_f32_e32 v18, v18
	v_mul_f32_e32 v16, 0x3fb8aa3b, v16
	v_sub_f32_e32 v14, v14, v35
	v_bitop3_b32 v13, v89, v13, s0 bitop3:0x78
	v_cndmask_b32_e64 v89, v211, -1, vcc
	v_cmp_lt_i32_e32 vcc, -1, v8
	v_add_f32_e32 v88, v88, v23
	v_exp_f32_e32 v16, v16
	v_mul_f32_e32 v14, 0x3fb8aa3b, v14
	v_sub_f32_e32 v13, v13, v35
	v_bitop3_b32 v11, v89, v11, s0 bitop3:0x78
	v_cndmask_b32_e64 v89, v211, -1, vcc
	v_add_f32_e32 v88, v88, v22
	v_exp_f32_e32 v14, v14
	v_mul_f32_e32 v13, 0x3fb8aa3b, v13
	v_sub_f32_e32 v11, v11, v35
	v_bitop3_b32 v8, v89, v8, s0 bitop3:0x78
	v_add_f32_e32 v88, v88, v20
	v_exp_f32_e32 v13, v13
	v_mul_f32_e32 v11, 0x3fb8aa3b, v11
	v_sub_f32_e32 v8, v8, v35
	v_add_f32_e32 v88, v88, v18
	v_exp_f32_e32 v11, v11
	v_mul_f32_e32 v8, 0x3fb8aa3b, v8
	v_add_f32_e32 v88, v88, v16
	v_exp_f32_e32 v8, v8
	v_add_f32_e32 v35, v88, v14
	v_add_f32_e32 v35, v35, v13
	v_add_f32_e32 v35, v35, v11
	v_add_f32_e32 v35, v35, v8
	v_div_scale_f32 v88, s[0:1], v35, v35, 1.0
	v_rcp_f32_e32 v89, v88
	s_waitcnt lgkmcnt(0)
	ds_write_b32 v25, v87 offset:4352
	ds_read_b32 v25, v86 offset:4352
	ds_add_rtn_u32 v86, v86, v0 offset:4608
	v_fma_f32 v90, -v88, v89, 1.0
	v_fmac_f32_e32 v89, v90, v89
	v_div_scale_f32 v90, vcc, 1.0, v35, 1.0
	v_mul_f32_e32 v91, v90, v89
	v_fma_f32 v92, -v88, v91, v90
	v_fmac_f32_e32 v91, v92, v89
	v_fma_f32 v88, -v88, v91, v90
	v_div_fmas_f32 v88, v88, v89, v91
	v_div_fixup_f32 v35, v88, v35, 1.0
	v_lshlrev_b32_e32 v1, 7, v1
	v_mul_f32_e32 v44, v44, v35
	s_waitcnt lgkmcnt(0)
	v_add3_u32 v25, v25, v1, v86
	s_waitcnt vmcnt(30)
	v_mul_f32_e32 v44, v68, v44
	v_lshl_add_u32 v25, v25, 2, s85
	ds_write_b32 v25, v44 offset:12288
	ds_write2st64_b32 v25, v66, v6 offset1:32
	ds_read_b32 v6, v85 offset:4352
	ds_add_rtn_u32 v25, v85, v0 offset:4608
	v_mul_f32_e32 v34, v34, v35
	s_waitcnt vmcnt(28)
	v_mul_f32_e32 v34, v67, v34
	s_mov_b32 s2, 0
	s_mov_b64 s[6:7], -1
	s_waitcnt lgkmcnt(0)
	v_add3_u32 v6, v6, v1, v25
	v_lshl_add_u32 v6, v6, 2, s85
	ds_write_b32 v6, v34 offset:12288
	ds_write2st64_b32 v6, v64, v5 offset1:32
	ds_read_b32 v5, v84 offset:4352
	ds_add_rtn_u32 v6, v84, v0 offset:4608
	v_mul_f32_e32 v25, v33, v35
	s_waitcnt vmcnt(26)
	v_mul_f32_e32 v25, v65, v25
	s_waitcnt lgkmcnt(0)
	v_add3_u32 v5, v5, v1, v6
	v_lshl_add_u32 v5, v5, 2, s85
	ds_write_b32 v5, v25 offset:12288
	ds_write2st64_b32 v5, v62, v4 offset1:32
	ds_read_b32 v4, v83 offset:4352
	ds_add_rtn_u32 v5, v83, v0 offset:4608
	v_mul_f32_e32 v6, v32, v35
	s_waitcnt vmcnt(24)
	v_mul_f32_e32 v6, v63, v6
	s_waitcnt lgkmcnt(0)
	v_add3_u32 v4, v4, v1, v5
	v_lshl_add_u32 v4, v4, 2, s85
	ds_write_b32 v4, v6 offset:12288
	ds_write2st64_b32 v4, v60, v2 offset1:32
	ds_read_b32 v2, v82 offset:4352
	ds_add_rtn_u32 v4, v82, v0 offset:4608
	v_mul_f32_e32 v5, v30, v35
	s_waitcnt vmcnt(22)
	v_mul_f32_e32 v5, v61, v5
	s_waitcnt lgkmcnt(0)
	v_add3_u32 v2, v2, v1, v4
	v_lshl_add_u32 v2, v2, 2, s85
	ds_write_b32 v2, v5 offset:12288
	ds_write2st64_b32 v2, v58, v12 offset1:32
	ds_read_b32 v2, v81 offset:4352
	ds_add_rtn_u32 v4, v81, v0 offset:4608
	v_mul_f32_e32 v5, v28, v35
	s_waitcnt vmcnt(20)
	v_mul_f32_e32 v5, v59, v5
	s_waitcnt lgkmcnt(0)
	v_add3_u32 v2, v2, v1, v4
	v_lshl_add_u32 v2, v2, 2, s85
	ds_write_b32 v2, v5 offset:12288
	ds_write2st64_b32 v2, v56, v10 offset1:32
	ds_read_b32 v2, v80 offset:4352
	ds_add_rtn_u32 v4, v80, v0 offset:4608
	v_mul_f32_e32 v5, v26, v35
	s_waitcnt vmcnt(18)
	v_mul_f32_e32 v5, v57, v5
	s_waitcnt lgkmcnt(0)
	v_add3_u32 v2, v2, v1, v4
	v_lshl_add_u32 v2, v2, 2, s85
	ds_write_b32 v2, v5 offset:12288
	ds_write2st64_b32 v2, v54, v9 offset1:32
	ds_read_b32 v2, v79 offset:4352
	ds_add_rtn_u32 v4, v79, v0 offset:4608
	v_mul_f32_e32 v5, v23, v35
	s_waitcnt vmcnt(16)
	v_mul_f32_e32 v5, v55, v5
	s_waitcnt lgkmcnt(0)
	v_add3_u32 v2, v2, v1, v4
	v_lshl_add_u32 v2, v2, 2, s85
	ds_write_b32 v2, v5 offset:12288
	ds_write2st64_b32 v2, v52, v7 offset1:32
	ds_read_b32 v2, v78 offset:4352
	ds_add_rtn_u32 v4, v78, v0 offset:4608
	v_mul_f32_e32 v5, v22, v35
	s_waitcnt vmcnt(14)
	v_mul_f32_e32 v5, v53, v5
	s_waitcnt lgkmcnt(0)
	v_add3_u32 v2, v2, v1, v4
	v_lshl_add_u32 v2, v2, 2, s85
	ds_write_b32 v2, v5 offset:12288
	ds_write2st64_b32 v2, v50, v21 offset1:32
	ds_read_b32 v2, v75 offset:4352
	ds_add_rtn_u32 v4, v75, v0 offset:4608
	v_mul_f32_e32 v5, v20, v35
	s_waitcnt vmcnt(12)
	v_mul_f32_e32 v5, v51, v5
	s_waitcnt lgkmcnt(0)
	v_add3_u32 v2, v2, v1, v4
	v_lshl_add_u32 v2, v2, 2, s85
	ds_write_b32 v2, v5 offset:12288
	ds_write2st64_b32 v2, v48, v19 offset1:32
	ds_read_b32 v2, v74 offset:4352
	ds_add_rtn_u32 v4, v74, v0 offset:4608
	v_mul_f32_e32 v5, v18, v35
	s_waitcnt vmcnt(10)
	v_mul_f32_e32 v5, v49, v5
	s_waitcnt lgkmcnt(0)
	v_add3_u32 v2, v2, v1, v4
	v_lshl_add_u32 v2, v2, 2, s85
	ds_write_b32 v2, v5 offset:12288
	ds_write2st64_b32 v2, v46, v17 offset1:32
	ds_read_b32 v2, v73 offset:4352
	ds_add_rtn_u32 v4, v73, v0 offset:4608
	v_mul_f32_e32 v5, v16, v35
	s_waitcnt vmcnt(8)
	v_mul_f32_e32 v5, v47, v5
	s_waitcnt lgkmcnt(0)
	v_add3_u32 v2, v2, v1, v4
	v_lshl_add_u32 v2, v2, 2, s85
	ds_write_b32 v2, v5 offset:12288
	ds_write2st64_b32 v2, v43, v15 offset1:32
	ds_read_b32 v2, v72 offset:4352
	ds_add_rtn_u32 v4, v72, v0 offset:4608
	v_mul_f32_e32 v5, v14, v35
	s_waitcnt vmcnt(6)
	v_mul_f32_e32 v5, v45, v5
	s_waitcnt lgkmcnt(0)
	v_add3_u32 v2, v2, v1, v4
	v_lshl_add_u32 v2, v2, 2, s85
	ds_write_b32 v2, v5 offset:12288
	ds_write2st64_b32 v2, v41, v31 offset1:32
	ds_read_b32 v2, v71 offset:4352
	ds_add_rtn_u32 v4, v71, v0 offset:4608
	v_mul_f32_e32 v5, v13, v35
	s_waitcnt vmcnt(4)
	v_mul_f32_e32 v5, v42, v5
	s_waitcnt lgkmcnt(0)
	v_add3_u32 v2, v2, v1, v4
	v_lshl_add_u32 v2, v2, 2, s85
	ds_write_b32 v2, v5 offset:12288
	ds_write2st64_b32 v2, v39, v29 offset1:32
	ds_read_b32 v2, v70 offset:4352
	ds_add_rtn_u32 v4, v70, v0 offset:4608
	v_mul_f32_e32 v5, v11, v35
	s_waitcnt vmcnt(2)
	v_mul_f32_e32 v5, v40, v5
	s_waitcnt lgkmcnt(0)
	v_add3_u32 v2, v2, v1, v4
	v_lshl_add_u32 v2, v2, 2, s85
	ds_write_b32 v2, v5 offset:12288
	ds_write2st64_b32 v2, v37, v27 offset1:32
	ds_read_b32 v2, v69 offset:4352
	ds_add_rtn_u32 v4, v69, v0 offset:4608
	v_mul_f32_e32 v5, v8, v35
	s_waitcnt vmcnt(0)
	v_mul_f32_e32 v5, v38, v5
	s_waitcnt lgkmcnt(0)
	v_add3_u32 v1, v2, v1, v4
	v_lshl_add_u32 v1, v1, 2, s85
	ds_write_b32 v1, v5 offset:12288
	ds_write2st64_b32 v1, v36, v24 offset1:32
	v_lshrrev_b32_e32 v5, 3, v178
	v_and_b32_e32 v6, 7, v178
	v_lshlrev_b32_e32 v7, 7, v5
	v_lshl_add_u32 v7, v6, 4, v7
	v_lshl_add_u32 v4, v7, 2, s85
	v_add_u32_e32 v4, 0x2000, v4
	ds_read2_b32 v[8:9], v4 offset1:8
	v_lshlrev_b32_e32 v12, 14, v5
	v_or_b32_e32 v12, v12, v7
	v_or_b32_e32 v12, 0x2000, v12
	v_mov_b32_e32 v10, 0
	v_mov_b32_e32 v11, 0
	s_mov_b32 s14, 0
	s_waitcnt lgkmcnt(0)
	v_bfe_u32 v8, v8, 11, 3
	v_bfe_u32 v9, v9, 11, 3
	v_cmp_eq_u32_e64 s[40:41], 0, v8
	v_cmp_eq_u32_e64 s[44:45], 0, v9
	s_nop 1
	v_mbcnt_lo_u32_b32 v13, s40, 0
	v_mbcnt_hi_u32_b32 v13, s41, v13
	v_mbcnt_lo_u32_b32 v13, s44, v13
	v_mbcnt_hi_u32_b32 v13, s45, v13
	v_add_u32_e32 v13, s14, v13
	v_cndmask_b32_e64 v10, v10, v13, s[40:41]
	v_cndmask_b32_e64 v14, 0, 1, s[40:41]
	v_add_u32_e32 v14, v13, v14
	v_cndmask_b32_e64 v11, v11, v14, s[44:45]
	s_bcnt1_i32_b64 s15, s[40:41]
	s_add_i32 s14, s14, s15
	s_bcnt1_i32_b64 s15, s[44:45]
	s_add_i32 s14, s14, s15
	v_cmp_eq_u32_e64 s[40:41], 1, v8
	v_cmp_eq_u32_e64 s[44:45], 1, v9
	s_nop 1
	v_mbcnt_lo_u32_b32 v13, s40, 0
	v_mbcnt_hi_u32_b32 v13, s41, v13
	v_mbcnt_lo_u32_b32 v13, s44, v13
	v_mbcnt_hi_u32_b32 v13, s45, v13
	v_add_u32_e32 v13, s14, v13
	v_cndmask_b32_e64 v10, v10, v13, s[40:41]
	v_cndmask_b32_e64 v14, 0, 1, s[40:41]
	v_add_u32_e32 v14, v13, v14
	v_cndmask_b32_e64 v11, v11, v14, s[44:45]
	s_bcnt1_i32_b64 s15, s[40:41]
	s_add_i32 s14, s14, s15
	s_bcnt1_i32_b64 s15, s[44:45]
	s_add_i32 s14, s14, s15
	v_cmp_eq_u32_e64 s[40:41], 2, v8
	v_cmp_eq_u32_e64 s[44:45], 2, v9
	s_nop 1
	v_mbcnt_lo_u32_b32 v13, s40, 0
	v_mbcnt_hi_u32_b32 v13, s41, v13
	v_mbcnt_lo_u32_b32 v13, s44, v13
	v_mbcnt_hi_u32_b32 v13, s45, v13
	v_add_u32_e32 v13, s14, v13
	v_cndmask_b32_e64 v10, v10, v13, s[40:41]
	v_cndmask_b32_e64 v14, 0, 1, s[40:41]
	v_add_u32_e32 v14, v13, v14
	v_cndmask_b32_e64 v11, v11, v14, s[44:45]
	s_bcnt1_i32_b64 s15, s[40:41]
	s_add_i32 s14, s14, s15
	s_bcnt1_i32_b64 s15, s[44:45]
	s_add_i32 s14, s14, s15
	v_cmp_eq_u32_e64 s[40:41], 3, v8
	v_cmp_eq_u32_e64 s[44:45], 3, v9
	s_nop 1
	v_mbcnt_lo_u32_b32 v13, s40, 0
	v_mbcnt_hi_u32_b32 v13, s41, v13
	v_mbcnt_lo_u32_b32 v13, s44, v13
	v_mbcnt_hi_u32_b32 v13, s45, v13
	v_add_u32_e32 v13, s14, v13
	v_cndmask_b32_e64 v10, v10, v13, s[40:41]
	v_cndmask_b32_e64 v14, 0, 1, s[40:41]
	v_add_u32_e32 v14, v13, v14
	v_cndmask_b32_e64 v11, v11, v14, s[44:45]
	s_bcnt1_i32_b64 s15, s[40:41]
	s_add_i32 s14, s14, s15
	s_bcnt1_i32_b64 s15, s[44:45]
	s_add_i32 s14, s14, s15
	v_cmp_eq_u32_e64 s[40:41], 4, v8
	v_cmp_eq_u32_e64 s[44:45], 4, v9
	s_nop 1
	v_mbcnt_lo_u32_b32 v13, s40, 0
	v_mbcnt_hi_u32_b32 v13, s41, v13
	v_mbcnt_lo_u32_b32 v13, s44, v13
	v_mbcnt_hi_u32_b32 v13, s45, v13
	v_add_u32_e32 v13, s14, v13
	v_cndmask_b32_e64 v10, v10, v13, s[40:41]
	v_cndmask_b32_e64 v14, 0, 1, s[40:41]
	v_add_u32_e32 v14, v13, v14
	v_cndmask_b32_e64 v11, v11, v14, s[44:45]
	s_bcnt1_i32_b64 s15, s[40:41]
	s_add_i32 s14, s14, s15
	s_bcnt1_i32_b64 s15, s[44:45]
	s_add_i32 s14, s14, s15
	v_cmp_eq_u32_e64 s[40:41], 5, v8
	v_cmp_eq_u32_e64 s[44:45], 5, v9
	s_nop 1
	v_mbcnt_lo_u32_b32 v13, s40, 0
	v_mbcnt_hi_u32_b32 v13, s41, v13
	v_mbcnt_lo_u32_b32 v13, s44, v13
	v_mbcnt_hi_u32_b32 v13, s45, v13
	v_add_u32_e32 v13, s14, v13
	v_cndmask_b32_e64 v10, v10, v13, s[40:41]
	v_cndmask_b32_e64 v14, 0, 1, s[40:41]
	v_add_u32_e32 v14, v13, v14
	v_cndmask_b32_e64 v11, v11, v14, s[44:45]
	s_bcnt1_i32_b64 s15, s[40:41]
	s_add_i32 s14, s14, s15
	s_bcnt1_i32_b64 s15, s[44:45]
	s_add_i32 s14, s14, s15
	v_cmp_eq_u32_e64 s[40:41], 6, v8
	v_cmp_eq_u32_e64 s[44:45], 6, v9
	s_nop 1
	v_mbcnt_lo_u32_b32 v13, s40, 0
	v_mbcnt_hi_u32_b32 v13, s41, v13
	v_mbcnt_lo_u32_b32 v13, s44, v13
	v_mbcnt_hi_u32_b32 v13, s45, v13
	v_add_u32_e32 v13, s14, v13
	v_cndmask_b32_e64 v10, v10, v13, s[40:41]
	v_cndmask_b32_e64 v14, 0, 1, s[40:41]
	v_add_u32_e32 v14, v13, v14
	v_cndmask_b32_e64 v11, v11, v14, s[44:45]
	s_bcnt1_i32_b64 s15, s[40:41]
	s_add_i32 s14, s14, s15
	s_bcnt1_i32_b64 s15, s[44:45]
	s_add_i32 s14, s14, s15
	v_cmp_eq_u32_e64 s[40:41], 7, v8
	v_cmp_eq_u32_e64 s[44:45], 7, v9
	s_nop 1
	v_mbcnt_lo_u32_b32 v13, s40, 0
	v_mbcnt_hi_u32_b32 v13, s41, v13
	v_mbcnt_lo_u32_b32 v13, s44, v13
	v_mbcnt_hi_u32_b32 v13, s45, v13
	v_add_u32_e32 v13, s14, v13
	v_cndmask_b32_e64 v10, v10, v13, s[40:41]
	v_cndmask_b32_e64 v14, 0, 1, s[40:41]
	v_add_u32_e32 v14, v13, v14
	v_cndmask_b32_e64 v11, v11, v14, s[44:45]
	s_bcnt1_i32_b64 s15, s[40:41]
	s_add_i32 s14, s14, s15
	s_bcnt1_i32_b64 s15, s[44:45]
	s_add_i32 s14, s14, s15
	v_lshl_add_u32 v10, v10, 2, s85
	v_lshl_add_u32 v11, v11, 2, s85
	v_add_u32_e32 v13, 8, v12
	ds_write_b32 v10, v12 offset:4864
	ds_write_b32 v11, v13 offset:4864
	s_movk_i32 s22, 0x80
	s_waitcnt lgkmcnt(0)
	s_waitcnt vmcnt(0)
	v_mov_b32_e32 v1, s85
	ds_read_b32 v1, v1 offset:4864
	s_mov_b32 s0, s33
	s_ashr_i32 s1, s33, 31
	s_lshl_b64 s[0:1], s[0:1], 11
	s_waitcnt lgkmcnt(0)
	v_readfirstlane_b32 s26, v1
	v_lshl_add_u64 v[142:143], v[76:77], 0, s[0:1]
	s_movk_i32 s88, 0
	v_lshl_add_u64 v[12:13], v[142:143], 0, s[88:89]
	global_load_dwordx4 v[78:81], v[12:13], off offset:0
	global_load_dwordx4 v[82:85], v[12:13], off offset:16
	global_load_dwordx4 v[86:89], v[12:13], off offset:2048
	global_load_dwordx4 v[90:93], v[12:13], off offset:2064
	s_movk_i32 s88, 4096
	v_lshl_add_u64 v[12:13], v[142:143], 0, s[88:89]
	global_load_dwordx4 v[94:97], v[12:13], off offset:0
	global_load_dwordx4 v[98:101], v[12:13], off offset:16
	global_load_dwordx4 v[102:105], v[12:13], off offset:2048
	global_load_dwordx4 v[106:109], v[12:13], off offset:2064
	s_movk_i32 s88, 8192
	v_lshl_add_u64 v[12:13], v[142:143], 0, s[88:89]
	global_load_dwordx4 v[110:113], v[12:13], off offset:0
	global_load_dwordx4 v[114:117], v[12:13], off offset:16
	global_load_dwordx4 v[118:121], v[12:13], off offset:2048
	global_load_dwordx4 v[122:125], v[12:13], off offset:2064
	s_movk_i32 s88, 12288
	v_lshl_add_u64 v[12:13], v[142:143], 0, s[88:89]
	global_load_dwordx4 v[126:129], v[12:13], off offset:0
	global_load_dwordx4 v[130:133], v[12:13], off offset:16
	global_load_dwordx4 v[134:137], v[12:13], off offset:2048
	global_load_dwordx4 v[138:141], v[12:13], off offset:2064
	s_mov_b32 s88, 0
	s_and_b32 s2, s26, 0x3ff
	s_bfe_u32 s3, s26, 0x4000a
	v_cmp_gt_u32_e32 vcc, s3, v182
	s_lshl_b32 s2, s2, 2
	s_add_i32 s2, s2, s85
	v_cndmask_b32_e32 v1, 0, v182, vcc
	v_lshl_add_u32 v1, v1, 2, s2
	ds_read_b32 v1, v1 offset:8192
	s_waitcnt lgkmcnt(0)
	v_lshlrev_b32_e32 v1, 10, v1
	v_and_b32_e32 v1, 0x3fffc00, v1
	s_nop 0
	v_readlane_b32 s44, v1, 0
	v_readlane_b32 s45, v1, 1
	v_readlane_b32 s46, v1, 2
	v_readlane_b32 s47, v1, 3
	v_readlane_b32 s48, v1, 4
	v_readlane_b32 s49, v1, 5
	v_readlane_b32 s50, v1, 6
	v_readlane_b32 s51, v1, 7
	s_nop 4
	buffer_load_dwordx4 v[68:71], v181, s[8:11], s44 offen
	buffer_load_dwordx4 v[64:67], v181, s[8:11], s45 offen
	buffer_load_dwordx4 v[60:63], v181, s[8:11], s46 offen
	buffer_load_dwordx4 v[56:59], v181, s[8:11], s47 offen
	buffer_load_dwordx4 v[48:51], v181, s[8:11], s48 offen
	buffer_load_dwordx4 v[32:35], v181, s[8:11], s49 offen
	buffer_load_dwordx4 v[16:19], v181, s[8:11], s50 offen
	buffer_load_dwordx4 v[12:15], v181, s[8:11], s51 offen
	s_add_i32 s3, s22, -1
	s_min_i32 s2, s3, 1
	s_max_i32 s2, s2, 0
	s_lshl_b32 s2, s2, 2
	s_add_i32 s2, s85, s2
	v_mov_b32_e32 v1, s2
	ds_read_b32 v1, v1 offset:4864
	s_waitcnt lgkmcnt(0)
	v_readfirstlane_b32 s86, v1
	s_and_b32 s2, s86, 0x3ff
	s_bfe_u32 s3, s86, 0x4000a
	v_cmp_gt_u32_e32 vcc, s3, v182
	s_lshl_b32 s2, s2, 2
	s_add_i32 s2, s2, s85
	v_cndmask_b32_e32 v1, 0, v182, vcc
	v_lshl_add_u32 v1, v1, 2, s2
	ds_read_b32 v1, v1 offset:8192
	s_waitcnt lgkmcnt(0)
	v_lshlrev_b32_e32 v1, 10, v1
	v_and_b32_e32 v1, 0x3fffc00, v1
	s_nop 0
	v_readlane_b32 s44, v1, 0
	v_readlane_b32 s45, v1, 1
	v_readlane_b32 s46, v1, 2
	v_readlane_b32 s47, v1, 3
	v_readlane_b32 s48, v1, 4
	v_readlane_b32 s49, v1, 5
	v_readlane_b32 s50, v1, 6
	v_readlane_b32 s51, v1, 7
	s_nop 4
	buffer_load_dwordx4 v[72:75], v181, s[8:11], s44 offen
	buffer_load_dwordx4 v[52:55], v181, s[8:11], s45 offen
	buffer_load_dwordx4 v[44:47], v181, s[8:11], s46 offen
	buffer_load_dwordx4 v[40:43], v181, s[8:11], s47 offen
	buffer_load_dwordx4 v[36:39], v181, s[8:11], s48 offen
	buffer_load_dwordx4 v[28:31], v181, s[8:11], s49 offen
	buffer_load_dwordx4 v[24:27], v181, s[8:11], s50 offen
	buffer_load_dwordx4 v[20:23], v181, s[8:11], s51 offen
	s_add_i32 s3, s22, -1
	s_min_i32 s2, s3, 2
	s_max_i32 s2, s2, 0
	s_lshl_b32 s2, s2, 2
	s_add_i32 s2, s85, s2
	v_mov_b32_e32 v1, s2
	ds_read_b32 v1, v1 offset:4864
	s_waitcnt lgkmcnt(0)
	v_readfirstlane_b32 s27, v1
	s_and_b32 s2, s27, 0x3ff
	s_bfe_u32 s3, s27, 0x4000a
	v_cmp_gt_u32_e32 vcc, s3, v182
	s_lshl_b32 s2, s2, 2
	s_add_i32 s2, s2, s85
	v_cndmask_b32_e32 v1, 0, v182, vcc
	v_lshl_add_u32 v1, v1, 2, s2
	ds_read_b32 v1, v1 offset:8192
	s_waitcnt lgkmcnt(0)
	v_lshlrev_b32_e32 v1, 10, v1
	v_and_b32_e32 v1, 0x3fffc00, v1
	s_nop 0
	v_readlane_b32 s44, v1, 0
	v_readlane_b32 s45, v1, 1
	v_readlane_b32 s46, v1, 2
	v_readlane_b32 s47, v1, 3
	v_readlane_b32 s48, v1, 4
	v_readlane_b32 s49, v1, 5
	v_readlane_b32 s50, v1, 6
	v_readlane_b32 s51, v1, 7
	s_nop 4
	buffer_load_dwordx4 v[224:227], v181, s[8:11], s44 offen
	buffer_load_dwordx4 v[228:231], v181, s[8:11], s45 offen
	buffer_load_dwordx4 v[232:235], v181, s[8:11], s46 offen
	buffer_load_dwordx4 v[236:239], v181, s[8:11], s47 offen
	buffer_load_dwordx4 v[240:243], v181, s[8:11], s48 offen
	buffer_load_dwordx4 v[244:247], v181, s[8:11], s49 offen
	buffer_load_dwordx4 v[248:251], v181, s[8:11], s50 offen
	buffer_load_dwordx4 v[216:219], v181, s[8:11], s51 offen
	s_add_i32 s3, s22, -1
	s_min_i32 s2, s3, 3
	s_max_i32 s2, s2, 0
	s_lshl_b32 s2, s2, 2
	s_add_i32 s2, s85, s2
	v_mov_b32_e32 v1, s2
	ds_read_b32 v1, v1 offset:4864
	s_waitcnt lgkmcnt(0)
	v_readfirstlane_b32 s32, v1
	s_mov_b32 s23, 0
	s_mov_b64 s[0:1], -1
